# v59 + the five GEMM K-loop heads and the two conversion loop heads aligned to 64 bytes (code placement pin, no instruction changes)
# speedup vs baseline: 1.0015x; 1.0015x over previous
.LBB0_106:
	s_add_u32 s24, s22, 0xf00
	s_addc_u32 s25, s23, 0
	s_and_b64 s[20:21], s[20:21], exec
	ds_write_b128 v195, v[0:3]
	s_cselect_b32 s20, s18, s24
	s_cselect_b32 s21, s19, s25
	s_add_u32 s51, s22, 0x100
	v_mov_b32_e32 v0, 0
	s_addc_u32 s52, s23, 0
	s_mov_b32 s53, -2
	s_mov_b64 s[22:23], 0
	v_mov_b32_e32 v1, v0
	v_mov_b32_e32 v2, v0
	v_mov_b32_e32 v3, v0
	v_mov_b32_e32 v4, v0
	v_mov_b32_e32 v5, v0
	v_mov_b32_e32 v6, v0
	v_mov_b32_e32 v7, v0
	v_mov_b32_e32 v16, v0
	v_mov_b32_e32 v17, v0
	v_mov_b32_e32 v18, v0
	v_mov_b32_e32 v19, v0
	v_mov_b32_e32 v20, v0
	v_mov_b32_e32 v21, v0
	v_mov_b32_e32 v22, v0
	v_mov_b32_e32 v23, v0
	v_mov_b32_e32 v32, v0
	v_mov_b32_e32 v33, v0
	v_mov_b32_e32 v34, v0
	v_mov_b32_e32 v35, v0
	v_mov_b32_e32 v36, v0
	v_mov_b32_e32 v37, v0
	v_mov_b32_e32 v38, v0
	v_mov_b32_e32 v39, v0
	v_mov_b32_e32 v48, v0
	v_mov_b32_e32 v49, v0
	v_mov_b32_e32 v50, v0
	v_mov_b32_e32 v51, v0
	v_mov_b32_e32 v52, v0
	v_mov_b32_e32 v53, v0
	v_mov_b32_e32 v54, v0
	v_mov_b32_e32 v55, v0
	v_mov_b32_e32 v8, v0
	v_mov_b32_e32 v9, v0
	v_mov_b32_e32 v10, v0
	v_mov_b32_e32 v11, v0
	v_mov_b32_e32 v12, v0
	v_mov_b32_e32 v13, v0
	v_mov_b32_e32 v14, v0
	v_mov_b32_e32 v15, v0
	v_mov_b32_e32 v24, v0
	v_mov_b32_e32 v25, v0
	v_mov_b32_e32 v26, v0
	v_mov_b32_e32 v27, v0
	v_mov_b32_e32 v28, v0
	v_mov_b32_e32 v29, v0
	v_mov_b32_e32 v30, v0
	v_mov_b32_e32 v31, v0
	v_mov_b32_e32 v40, v0
	v_mov_b32_e32 v41, v0
	v_mov_b32_e32 v42, v0
	v_mov_b32_e32 v43, v0
	v_mov_b32_e32 v44, v0
	v_mov_b32_e32 v45, v0
	v_mov_b32_e32 v46, v0
	v_mov_b32_e32 v47, v0
	v_mov_b32_e32 v56, v0
	v_mov_b32_e32 v57, v0
	v_mov_b32_e32 v58, v0
	v_mov_b32_e32 v59, v0
	v_mov_b32_e32 v60, v0
	v_mov_b32_e32 v61, v0
	v_mov_b32_e32 v62, v0
	v_mov_b32_e32 v63, v0
	v_mov_b32_e32 v68, v0
	v_mov_b32_e32 v69, v0
	v_mov_b32_e32 v70, v0
	v_mov_b32_e32 v71, v0
	v_mov_b32_e32 v72, v0
	v_mov_b32_e32 v73, v0
	v_mov_b32_e32 v74, v0
	v_mov_b32_e32 v75, v0
	v_mov_b32_e32 v84, v0
	v_mov_b32_e32 v85, v0
	v_mov_b32_e32 v86, v0
	v_mov_b32_e32 v87, v0
	v_mov_b32_e32 v88, v0
	v_mov_b32_e32 v89, v0
	v_mov_b32_e32 v90, v0
	v_mov_b32_e32 v91, v0
	v_mov_b32_e32 v100, v0
	v_mov_b32_e32 v101, v0
	v_mov_b32_e32 v102, v0
	v_mov_b32_e32 v103, v0
	v_mov_b32_e32 v104, v0
	v_mov_b32_e32 v105, v0
	v_mov_b32_e32 v106, v0
	v_mov_b32_e32 v107, v0
	v_mov_b32_e32 v116, v0
	v_mov_b32_e32 v117, v0
	v_mov_b32_e32 v118, v0
	v_mov_b32_e32 v119, v0
	v_mov_b32_e32 v120, v0
	v_mov_b32_e32 v121, v0
	v_mov_b32_e32 v122, v0
	v_mov_b32_e32 v123, v0
	v_mov_b32_e32 v76, v0
	v_mov_b32_e32 v77, v0
	v_mov_b32_e32 v78, v0
	v_mov_b32_e32 v79, v0
	v_mov_b32_e32 v80, v0
	v_mov_b32_e32 v81, v0
	v_mov_b32_e32 v82, v0
	v_mov_b32_e32 v83, v0
	v_mov_b32_e32 v92, v0
	v_mov_b32_e32 v93, v0
	v_mov_b32_e32 v94, v0
	v_mov_b32_e32 v95, v0
	v_mov_b32_e32 v96, v0
	v_mov_b32_e32 v97, v0
	v_mov_b32_e32 v98, v0
	v_mov_b32_e32 v99, v0
	v_mov_b32_e32 v108, v0
	v_mov_b32_e32 v109, v0
	v_mov_b32_e32 v110, v0
	v_mov_b32_e32 v111, v0
	v_mov_b32_e32 v112, v0
	v_mov_b32_e32 v113, v0
	v_mov_b32_e32 v114, v0
	v_mov_b32_e32 v115, v0
	v_mov_b32_e32 v124, v0
	v_mov_b32_e32 v125, v0
	v_mov_b32_e32 v126, v0
	v_mov_b32_e32 v127, v0
	v_mov_b32_e32 v128, v0
	v_mov_b32_e32 v129, v0
	v_mov_b32_e32 v130, v0
	v_mov_b32_e32 v131, v0
	s_branch .LBB0_108
	.p2alignl 6, 3212836864

.Lcva_ga167:
	global_load_dwordx4 v[98:101], v130, s[0:1] nt
	global_load_dwordx4 v[102:105], v131, s[0:1] nt
	global_load_dwordx4 v[106:109], v132, s[0:1] nt
	global_load_dwordx4 v[110:113], v133, s[0:1] nt
	global_load_dwordx4 v[114:117], v134, s[0:1] nt
	global_load_dwordx4 v[118:121], v135, s[0:1] nt
	global_load_dwordx4 v[122:125], v136, s[0:1] nt
	global_load_dwordx4 v[126:129], v137, s[0:1] nt
	s_add_u32 s0, s0, 0x10000
	s_addc_u32 s1, s1, 0
	s_waitcnt vmcnt(16)
	v_pk_mul_f32 v[34:35], v[34:35], v[248:249]
	v_pk_mul_f32 v[36:37], v[36:37], v[248:249]
	v_pk_mul_f32 v[38:39], v[38:39], v[248:249]
	v_pk_mul_f32 v[40:41], v[40:41], v[248:249]
	v_pk_mul_f32 v[42:43], v[42:43], v[248:249]
	v_pk_mul_f32 v[44:45], v[44:45], v[248:249]
	v_pk_mul_f32 v[46:47], v[46:47], v[248:249]
	v_pk_mul_f32 v[48:49], v[48:49], v[248:249]
	v_pk_mul_f32 v[50:51], v[50:51], v[248:249]
	v_pk_mul_f32 v[52:53], v[52:53], v[248:249]
	v_pk_mul_f32 v[54:55], v[54:55], v[248:249]
	v_pk_mul_f32 v[56:57], v[56:57], v[248:249]
	v_pk_mul_f32 v[58:59], v[58:59], v[248:249]
	v_pk_mul_f32 v[60:61], v[60:61], v[248:249]
	v_pk_mul_f32 v[62:63], v[62:63], v[248:249]
	v_pk_mul_f32 v[64:65], v[64:65], v[248:249]
	v_cvt_pk_fp8_f32 v208, v34, v38
	v_cvt_pk_fp8_f32 v209, v50, v54
	v_cvt_pk_fp8_f32 v210, v35, v39
	v_cvt_pk_fp8_f32 v211, v51, v55
	v_cvt_pk_fp8_f32 v212, v36, v40
	v_cvt_pk_fp8_f32 v213, v52, v56
	v_cvt_pk_fp8_f32 v214, v37, v41
	v_cvt_pk_fp8_f32 v215, v53, v57
	v_cvt_pk_fp8_f32 v208, v42, v46 op_sel:[0,0,1]
	v_cvt_pk_fp8_f32 v209, v58, v62 op_sel:[0,0,1]
	v_cvt_pk_fp8_f32 v210, v43, v47 op_sel:[0,0,1]
	v_cvt_pk_fp8_f32 v211, v59, v63 op_sel:[0,0,1]
	v_cvt_pk_fp8_f32 v212, v44, v48 op_sel:[0,0,1]
	v_cvt_pk_fp8_f32 v213, v60, v64 op_sel:[0,0,1]
	v_cvt_pk_fp8_f32 v214, v45, v49 op_sel:[0,0,1]
	v_cvt_pk_fp8_f32 v215, v61, v65 op_sel:[0,0,1]
	s_nop 0
	ds_write2_b64 v139, v[208:209], v[210:211] offset1:16
	ds_write2_b64 v139, v[212:213], v[214:215] offset0:32 offset1:48
	global_load_dwordx4 v[2:5], v130, s[0:1] nt
	global_load_dwordx4 v[6:9], v131, s[0:1] nt
	global_load_dwordx4 v[10:13], v132, s[0:1] nt
	global_load_dwordx4 v[14:17], v133, s[0:1] nt
	global_load_dwordx4 v[18:21], v134, s[0:1] nt
	global_load_dwordx4 v[22:25], v135, s[0:1] nt
	global_load_dwordx4 v[26:29], v136, s[0:1] nt
	global_load_dwordx4 v[30:33], v137, s[0:1] nt
	s_add_u32 s0, s0, 0x10000
	s_addc_u32 s1, s1, 0
	s_waitcnt vmcnt(16)
	v_pk_mul_f32 v[66:67], v[66:67], v[248:249]
	v_pk_mul_f32 v[68:69], v[68:69], v[248:249]
	v_pk_mul_f32 v[70:71], v[70:71], v[248:249]
	v_pk_mul_f32 v[72:73], v[72:73], v[248:249]
	v_pk_mul_f32 v[74:75], v[74:75], v[248:249]
	v_pk_mul_f32 v[76:77], v[76:77], v[248:249]
	v_pk_mul_f32 v[78:79], v[78:79], v[248:249]
	v_pk_mul_f32 v[80:81], v[80:81], v[248:249]
	v_pk_mul_f32 v[82:83], v[82:83], v[248:249]
	v_pk_mul_f32 v[84:85], v[84:85], v[248:249]
	v_pk_mul_f32 v[86:87], v[86:87], v[248:249]
	v_pk_mul_f32 v[88:89], v[88:89], v[248:249]
	v_pk_mul_f32 v[90:91], v[90:91], v[248:249]
	v_pk_mul_f32 v[92:93], v[92:93], v[248:249]
	v_pk_mul_f32 v[94:95], v[94:95], v[248:249]
	v_pk_mul_f32 v[96:97], v[96:97], v[248:249]
	v_cvt_pk_fp8_f32 v200, v66, v70
	v_cvt_pk_fp8_f32 v201, v82, v86
	v_cvt_pk_fp8_f32 v202, v67, v71
	v_cvt_pk_fp8_f32 v203, v83, v87
	v_cvt_pk_fp8_f32 v204, v68, v72
	v_cvt_pk_fp8_f32 v205, v84, v88
	v_cvt_pk_fp8_f32 v206, v69, v73
	v_cvt_pk_fp8_f32 v207, v85, v89
	v_cvt_pk_fp8_f32 v200, v74, v78 op_sel:[0,0,1]
	v_cvt_pk_fp8_f32 v201, v90, v94 op_sel:[0,0,1]
	v_cvt_pk_fp8_f32 v202, v75, v79 op_sel:[0,0,1]
	v_cvt_pk_fp8_f32 v203, v91, v95 op_sel:[0,0,1]
	v_cvt_pk_fp8_f32 v204, v76, v80 op_sel:[0,0,1]
	v_cvt_pk_fp8_f32 v205, v92, v96 op_sel:[0,0,1]
	v_cvt_pk_fp8_f32 v206, v77, v81 op_sel:[0,0,1]
	v_cvt_pk_fp8_f32 v207, v93, v97 op_sel:[0,0,1]
	s_nop 0
	ds_write2_b64 v140, v[200:201], v[202:203] offset1:16
	ds_write2_b64 v140, v[204:205], v[206:207] offset0:32 offset1:48
	global_load_dwordx4 v[34:37], v130, s[0:1] nt
	global_load_dwordx4 v[38:41], v131, s[0:1] nt
	global_load_dwordx4 v[42:45], v132, s[0:1] nt
	global_load_dwordx4 v[46:49], v133, s[0:1] nt
	global_load_dwordx4 v[50:53], v134, s[0:1] nt
	global_load_dwordx4 v[54:57], v135, s[0:1] nt
	global_load_dwordx4 v[58:61], v136, s[0:1] nt
	global_load_dwordx4 v[62:65], v137, s[0:1] nt
	s_add_u32 s0, s0, 0x10000
	s_addc_u32 s1, s1, 0
	s_branch .Lcva_s3
	.p2alignl 6, 3212836864

.LBB0_499:
	s_add_u32 s20, s18, 0xf00
	s_addc_u32 s21, s19, 0
	s_and_b64 s[14:15], s[14:15], exec
	ds_write_b128 v137, v[0:3]
	s_cselect_b32 s14, s12, s20
	s_cselect_b32 s15, s13, s21
	s_add_u32 s43, s18, 0x100
	v_mov_b32_e32 v0, 0
	s_addc_u32 s44, s19, 0
	s_mov_b32 s45, -2
	s_mov_b64 s[18:19], 0
	v_mov_b32_e32 v1, v0
	v_mov_b32_e32 v2, v0
	v_mov_b32_e32 v3, v0
	v_mov_b32_e32 v4, v0
	v_mov_b32_e32 v5, v0
	v_mov_b32_e32 v6, v0
	v_mov_b32_e32 v7, v0
	v_mov_b32_e32 v16, v0
	v_mov_b32_e32 v17, v0
	v_mov_b32_e32 v18, v0
	v_mov_b32_e32 v19, v0
	v_mov_b32_e32 v24, v0
	v_mov_b32_e32 v25, v0
	v_mov_b32_e32 v26, v0
	v_mov_b32_e32 v27, v0
	v_mov_b32_e32 v32, v0
	v_mov_b32_e32 v33, v0
	v_mov_b32_e32 v34, v0
	v_mov_b32_e32 v35, v0
	v_mov_b32_e32 v40, v0
	v_mov_b32_e32 v41, v0
	v_mov_b32_e32 v42, v0
	v_mov_b32_e32 v43, v0
	v_mov_b32_e32 v44, v0
	v_mov_b32_e32 v45, v0
	v_mov_b32_e32 v46, v0
	v_mov_b32_e32 v47, v0
	v_mov_b32_e32 v52, v0
	v_mov_b32_e32 v53, v0
	v_mov_b32_e32 v54, v0
	v_mov_b32_e32 v55, v0
	v_mov_b32_e32 v12, v0
	v_mov_b32_e32 v13, v0
	v_mov_b32_e32 v14, v0
	v_mov_b32_e32 v15, v0
	v_mov_b32_e32 v20, v0
	v_mov_b32_e32 v21, v0
	v_mov_b32_e32 v22, v0
	v_mov_b32_e32 v23, v0
	v_mov_b32_e32 v28, v0
	v_mov_b32_e32 v29, v0
	v_mov_b32_e32 v30, v0
	v_mov_b32_e32 v31, v0
	v_mov_b32_e32 v36, v0
	v_mov_b32_e32 v37, v0
	v_mov_b32_e32 v38, v0
	v_mov_b32_e32 v39, v0
	v_mov_b32_e32 v48, v0
	v_mov_b32_e32 v49, v0
	v_mov_b32_e32 v50, v0
	v_mov_b32_e32 v51, v0
	v_mov_b32_e32 v56, v0
	v_mov_b32_e32 v57, v0
	v_mov_b32_e32 v58, v0
	v_mov_b32_e32 v59, v0
	v_mov_b32_e32 v60, v0
	v_mov_b32_e32 v61, v0
	v_mov_b32_e32 v62, v0
	v_mov_b32_e32 v63, v0
	v_mov_b32_e32 v64, v0
	v_mov_b32_e32 v65, v0
	v_mov_b32_e32 v66, v0
	v_mov_b32_e32 v67, v0
	v_mov_b32_e32 v68, v0
	v_mov_b32_e32 v69, v0
	v_mov_b32_e32 v70, v0
	v_mov_b32_e32 v71, v0
	v_mov_b32_e32 v72, v0
	v_mov_b32_e32 v73, v0
	v_mov_b32_e32 v74, v0
	v_mov_b32_e32 v75, v0
	v_mov_b32_e32 v80, v0
	v_mov_b32_e32 v81, v0
	v_mov_b32_e32 v82, v0
	v_mov_b32_e32 v83, v0
	v_mov_b32_e32 v88, v0
	v_mov_b32_e32 v89, v0
	v_mov_b32_e32 v90, v0
	v_mov_b32_e32 v91, v0
	v_mov_b32_e32 v92, v0
	v_mov_b32_e32 v93, v0
	v_mov_b32_e32 v94, v0
	v_mov_b32_e32 v95, v0
	v_mov_b32_e32 v96, v0
	v_mov_b32_e32 v97, v0
	v_mov_b32_e32 v98, v0
	v_mov_b32_e32 v99, v0
	v_mov_b32_e32 v104, v0
	v_mov_b32_e32 v105, v0
	v_mov_b32_e32 v106, v0
	v_mov_b32_e32 v107, v0
	v_mov_b32_e32 v108, v0
	v_mov_b32_e32 v109, v0
	v_mov_b32_e32 v110, v0
	v_mov_b32_e32 v111, v0
	v_mov_b32_e32 v76, v0
	v_mov_b32_e32 v77, v0
	v_mov_b32_e32 v78, v0
	v_mov_b32_e32 v79, v0
	v_mov_b32_e32 v84, v0
	v_mov_b32_e32 v85, v0
	v_mov_b32_e32 v86, v0
	v_mov_b32_e32 v87, v0
	v_mov_b32_e32 v100, v0
	v_mov_b32_e32 v101, v0
	v_mov_b32_e32 v102, v0
	v_mov_b32_e32 v103, v0
	v_mov_b32_e32 v112, v0
	v_mov_b32_e32 v113, v0
	v_mov_b32_e32 v114, v0
	v_mov_b32_e32 v115, v0
	v_mov_b32_e32 v116, v0
	v_mov_b32_e32 v117, v0
	v_mov_b32_e32 v118, v0
	v_mov_b32_e32 v119, v0
	v_mov_b32_e32 v120, v0
	v_mov_b32_e32 v121, v0
	v_mov_b32_e32 v122, v0
	v_mov_b32_e32 v123, v0
	v_mov_b32_e32 v124, v0
	v_mov_b32_e32 v125, v0
	v_mov_b32_e32 v126, v0
	v_mov_b32_e32 v127, v0
	v_mov_b32_e32 v128, v0
	v_mov_b32_e32 v129, v0
	v_mov_b32_e32 v130, v0
	v_mov_b32_e32 v131, v0
	s_branch .LBB0_501
	.p2alignl 6, 3212836864

.LBB0_831:
	s_add_u32 s5, s18, 0x700
	s_addc_u32 s40, s19, 0
	s_and_b64 s[0:1], s[36:37], exec
	s_cselect_b32 s0, s30, s5
	s_cselect_b32 s1, s31, s40
	s_mov_b32 s5, -2
	s_mov_b64 s[40:41], 0x12800000
	ds_write_b128 v253, v[132:135]
	s_branch .LBB0_833
	.p2alignl 6, 3212836864

.Lcvc_entry:
	s_mov_b64 exec, -1
	v_readlane_b32 s26, v255, 4
	v_mbcnt_lo_u32_b32 v1, -1, 0
	v_mbcnt_hi_u32_b32 v1, -1, v1
	s_lshr_b32 s19, s26, 6
	s_lshr_b32 s20, s19, 2
	s_and_b32 s21, s19, 3
	s_lshl_b32 s25, s20, 19
	s_lshl_b32 s22, s21, 10
	s_add_u32 s25, s25, s22
	v_lshlrev_b32_e32 v130, 4, v1
	v_add_u32_e32 v131, 0x2000, v130
	v_add_u32_e32 v132, 0x4000, v130
	v_add_u32_e32 v133, 0x6000, v130
	v_add_u32_e32 v134, 0x8000, v130
	v_add_u32_e32 v135, 0xa000, v130
	v_add_u32_e32 v136, 0xc000, v130
	v_add_u32_e32 v137, 0xe000, v130
	v_and_b32_e32 v150, 15, v1
	s_lshl_b32 s22, s20, 3
	v_xor_b32_e32 v150, s22, v150
	v_lshlrev_b32_e32 v151, 9, v1
	s_lshl_b32 s22, s21, 15
	v_add_u32_e32 v151, s22, v151
	v_xor_b32_e32 v138, 0, v150
	v_lshl_add_u32 v138, v138, 3, v151
	v_xor_b32_e32 v139, 1, v150
	v_lshl_add_u32 v139, v139, 3, v151
	v_xor_b32_e32 v140, 2, v150
	v_lshl_add_u32 v140, v140, 3, v151
	v_xor_b32_e32 v141, 3, v150
	v_lshl_add_u32 v141, v141, 3, v151
	v_xor_b32_e32 v142, 4, v150
	v_lshl_add_u32 v142, v142, 3, v151
	v_xor_b32_e32 v143, 5, v150
	v_lshl_add_u32 v143, v143, 3, v151
	v_xor_b32_e32 v144, 6, v150
	v_lshl_add_u32 v144, v144, 3, v151
	v_xor_b32_e32 v145, 7, v150
	v_lshl_add_u32 v145, v145, 3, v151
	v_add_u32_e32 v152, s26, v1
	v_lshrrev_b32_e32 v153, 3, v152
	v_and_b32_e32 v154, 7, v152
	v_bfe_u32 v155, v152, 5, 4
	v_lshlrev_b32_e32 v156, 1, v154
	v_and_b32_e32 v157, 14, v155
	v_xor_b32_e32 v156, v156, v157
	v_lshlrev_b32_e32 v156, 3, v156
	v_lshl_add_u32 v146, v153, 7, v156
	v_add_u32_e32 v147, 0x10000, v146
	v_lshlrev_b32_e32 v148, 4, v154
	v_lshl_add_u32 v148, v153, 11, v148
	v_and_b32_e32 v157, 1, v155
	v_cmp_ne_u32_e64 s[30:31], 0, v157
	v_mov_b32_e32 v248, 0x42800000
	v_mov_b32_e32 v249, 0x42800000
	v_mov_b32_e32 v250, 0
	v_mov_b32_e32 v251, 1
	v_mov_b32_e32 v252, 0x20800
	s_waitcnt lgkmcnt(0)
	s_barrier
	s_cmp_ge_u32 s6, s24
	s_cbranch_scc1 .Lcvc_done
	s_lshr_b32 s19, s6, 10
	s_and_b32 s20, s6, 0x3ff
	s_cmp_eq_u32 s19, 0
	s_cselect_b32 s0, s34, s36
	s_cselect_b32 s1, s35, s37
	s_cmp_eq_u32 s19, 2
	s_cselect_b32 s0, s38, s0
	s_cselect_b32 s1, s39, s1
	s_lshr_b32 s21, s20, 5
	s_lshl_b32 s21, s21, 24
	s_bfe_u32 s22, s20, 0x40001
	s_lshl_b32 s22, s22, 20
	s_add_u32 s21, s21, s22
	s_and_b32 s22, s20, 1
	s_lshl_b32 s22, s22, 12
	s_add_u32 s21, s21, s22
	s_add_u32 s21, s21, s25
	s_add_u32 s0, s0, s21
	s_addc_u32 s1, s1, 0
	global_load_dwordx4 v[2:5], v130, s[0:1] nt
	global_load_dwordx4 v[6:9], v131, s[0:1] nt
	global_load_dwordx4 v[10:13], v132, s[0:1] nt
	global_load_dwordx4 v[14:17], v133, s[0:1] nt
	global_load_dwordx4 v[18:21], v134, s[0:1] nt
	global_load_dwordx4 v[22:25], v135, s[0:1] nt
	global_load_dwordx4 v[26:29], v136, s[0:1] nt
	global_load_dwordx4 v[30:33], v137, s[0:1] nt
	s_add_u32 s0, s0, 0x10000
	s_addc_u32 s1, s1, 0
	global_load_dwordx4 v[34:37], v130, s[0:1] nt
	global_load_dwordx4 v[38:41], v131, s[0:1] nt
	global_load_dwordx4 v[42:45], v132, s[0:1] nt
	global_load_dwordx4 v[46:49], v133, s[0:1] nt
	global_load_dwordx4 v[50:53], v134, s[0:1] nt
	global_load_dwordx4 v[54:57], v135, s[0:1] nt
	global_load_dwordx4 v[58:61], v136, s[0:1] nt
	global_load_dwordx4 v[62:65], v137, s[0:1] nt
	s_add_u32 s0, s0, 0x10000
	s_addc_u32 s1, s1, 0
	global_load_dwordx4 v[66:69], v130, s[0:1] nt
	global_load_dwordx4 v[70:73], v131, s[0:1] nt
	global_load_dwordx4 v[74:77], v132, s[0:1] nt
	global_load_dwordx4 v[78:81], v133, s[0:1] nt
	global_load_dwordx4 v[82:85], v134, s[0:1] nt
	global_load_dwordx4 v[86:89], v135, s[0:1] nt
	global_load_dwordx4 v[90:93], v136, s[0:1] nt
	global_load_dwordx4 v[94:97], v137, s[0:1] nt
	s_add_u32 s0, s0, 0x10000
	s_addc_u32 s1, s1, 0
	s_waitcnt vmcnt(16)
	v_pk_mul_f32 v[2:3], v[2:3], v[248:249]
	v_pk_mul_f32 v[4:5], v[4:5], v[248:249]
	v_pk_mul_f32 v[6:7], v[6:7], v[248:249]
	v_pk_mul_f32 v[8:9], v[8:9], v[248:249]
	v_pk_mul_f32 v[10:11], v[10:11], v[248:249]
	v_pk_mul_f32 v[12:13], v[12:13], v[248:249]
	v_pk_mul_f32 v[14:15], v[14:15], v[248:249]
	v_pk_mul_f32 v[16:17], v[16:17], v[248:249]
	v_pk_mul_f32 v[18:19], v[18:19], v[248:249]
	v_pk_mul_f32 v[20:21], v[20:21], v[248:249]
	v_pk_mul_f32 v[22:23], v[22:23], v[248:249]
	v_pk_mul_f32 v[24:25], v[24:25], v[248:249]
	v_pk_mul_f32 v[26:27], v[26:27], v[248:249]
	v_pk_mul_f32 v[28:29], v[28:29], v[248:249]
	v_pk_mul_f32 v[30:31], v[30:31], v[248:249]
	v_pk_mul_f32 v[32:33], v[32:33], v[248:249]
	v_cvt_pk_fp8_f32 v200, v2, v6
	v_cvt_pk_fp8_f32 v201, v18, v22
	v_cvt_pk_fp8_f32 v202, v3, v7
	v_cvt_pk_fp8_f32 v203, v19, v23
	v_cvt_pk_fp8_f32 v204, v4, v8
	v_cvt_pk_fp8_f32 v205, v20, v24
	v_cvt_pk_fp8_f32 v206, v5, v9
	v_cvt_pk_fp8_f32 v207, v21, v25
	v_cvt_pk_fp8_f32 v200, v10, v14 op_sel:[0,0,1]
	v_cvt_pk_fp8_f32 v201, v26, v30 op_sel:[0,0,1]
	v_cvt_pk_fp8_f32 v202, v11, v15 op_sel:[0,0,1]
	v_cvt_pk_fp8_f32 v203, v27, v31 op_sel:[0,0,1]
	v_cvt_pk_fp8_f32 v204, v12, v16 op_sel:[0,0,1]
	v_cvt_pk_fp8_f32 v205, v28, v32 op_sel:[0,0,1]
	v_cvt_pk_fp8_f32 v206, v13, v17 op_sel:[0,0,1]
	v_cvt_pk_fp8_f32 v207, v29, v33 op_sel:[0,0,1]
	s_nop 0
	ds_write2_b64 v138, v[200:201], v[202:203] offset1:16
	ds_write2_b64 v138, v[204:205], v[206:207] offset0:32 offset1:48
	global_load_dwordx4 v[98:101], v130, s[0:1] nt
	global_load_dwordx4 v[102:105], v131, s[0:1] nt
	global_load_dwordx4 v[106:109], v132, s[0:1] nt
	global_load_dwordx4 v[110:113], v133, s[0:1] nt
	global_load_dwordx4 v[114:117], v134, s[0:1] nt
	global_load_dwordx4 v[118:121], v135, s[0:1] nt
	global_load_dwordx4 v[122:125], v136, s[0:1] nt
	global_load_dwordx4 v[126:129], v137, s[0:1] nt
	s_add_u32 s0, s0, 0x10000
	s_addc_u32 s1, s1, 0
	s_waitcnt vmcnt(16)
	v_pk_mul_f32 v[34:35], v[34:35], v[248:249]
	v_pk_mul_f32 v[36:37], v[36:37], v[248:249]
	v_pk_mul_f32 v[38:39], v[38:39], v[248:249]
	v_pk_mul_f32 v[40:41], v[40:41], v[248:249]
	v_pk_mul_f32 v[42:43], v[42:43], v[248:249]
	v_pk_mul_f32 v[44:45], v[44:45], v[248:249]
	v_pk_mul_f32 v[46:47], v[46:47], v[248:249]
	v_pk_mul_f32 v[48:49], v[48:49], v[248:249]
	v_pk_mul_f32 v[50:51], v[50:51], v[248:249]
	v_pk_mul_f32 v[52:53], v[52:53], v[248:249]
	v_pk_mul_f32 v[54:55], v[54:55], v[248:249]
	v_pk_mul_f32 v[56:57], v[56:57], v[248:249]
	v_pk_mul_f32 v[58:59], v[58:59], v[248:249]
	v_pk_mul_f32 v[60:61], v[60:61], v[248:249]
	v_pk_mul_f32 v[62:63], v[62:63], v[248:249]
	v_pk_mul_f32 v[64:65], v[64:65], v[248:249]
	v_cvt_pk_fp8_f32 v208, v34, v38
	v_cvt_pk_fp8_f32 v209, v50, v54
	v_cvt_pk_fp8_f32 v210, v35, v39
	v_cvt_pk_fp8_f32 v211, v51, v55
	v_cvt_pk_fp8_f32 v212, v36, v40
	v_cvt_pk_fp8_f32 v213, v52, v56
	v_cvt_pk_fp8_f32 v214, v37, v41
	v_cvt_pk_fp8_f32 v215, v53, v57
	v_cvt_pk_fp8_f32 v208, v42, v46 op_sel:[0,0,1]
	v_cvt_pk_fp8_f32 v209, v58, v62 op_sel:[0,0,1]
	v_cvt_pk_fp8_f32 v210, v43, v47 op_sel:[0,0,1]
	v_cvt_pk_fp8_f32 v211, v59, v63 op_sel:[0,0,1]
	v_cvt_pk_fp8_f32 v212, v44, v48 op_sel:[0,0,1]
	v_cvt_pk_fp8_f32 v213, v60, v64 op_sel:[0,0,1]
	v_cvt_pk_fp8_f32 v214, v45, v49 op_sel:[0,0,1]
	v_cvt_pk_fp8_f32 v215, v61, v65 op_sel:[0,0,1]
	s_nop 0
	ds_write2_b64 v139, v[208:209], v[210:211] offset1:16
	ds_write2_b64 v139, v[212:213], v[214:215] offset0:32 offset1:48
	global_load_dwordx4 v[2:5], v130, s[0:1] nt
	global_load_dwordx4 v[6:9], v131, s[0:1] nt
	global_load_dwordx4 v[10:13], v132, s[0:1] nt
	global_load_dwordx4 v[14:17], v133, s[0:1] nt
	global_load_dwordx4 v[18:21], v134, s[0:1] nt
	global_load_dwordx4 v[22:25], v135, s[0:1] nt
	global_load_dwordx4 v[26:29], v136, s[0:1] nt
	global_load_dwordx4 v[30:33], v137, s[0:1] nt
	s_add_u32 s0, s0, 0x10000
	s_addc_u32 s1, s1, 0
	s_waitcnt vmcnt(16)
	v_pk_mul_f32 v[66:67], v[66:67], v[248:249]
	v_pk_mul_f32 v[68:69], v[68:69], v[248:249]
	v_pk_mul_f32 v[70:71], v[70:71], v[248:249]
	v_pk_mul_f32 v[72:73], v[72:73], v[248:249]
	v_pk_mul_f32 v[74:75], v[74:75], v[248:249]
	v_pk_mul_f32 v[76:77], v[76:77], v[248:249]
	v_pk_mul_f32 v[78:79], v[78:79], v[248:249]
	v_pk_mul_f32 v[80:81], v[80:81], v[248:249]
	v_pk_mul_f32 v[82:83], v[82:83], v[248:249]
	v_pk_mul_f32 v[84:85], v[84:85], v[248:249]
	v_pk_mul_f32 v[86:87], v[86:87], v[248:249]
	v_pk_mul_f32 v[88:89], v[88:89], v[248:249]
	v_pk_mul_f32 v[90:91], v[90:91], v[248:249]
	v_pk_mul_f32 v[92:93], v[92:93], v[248:249]
	v_pk_mul_f32 v[94:95], v[94:95], v[248:249]
	v_pk_mul_f32 v[96:97], v[96:97], v[248:249]
	v_cvt_pk_fp8_f32 v200, v66, v70
	v_cvt_pk_fp8_f32 v201, v82, v86
	v_cvt_pk_fp8_f32 v202, v67, v71
	v_cvt_pk_fp8_f32 v203, v83, v87
	v_cvt_pk_fp8_f32 v204, v68, v72
	v_cvt_pk_fp8_f32 v205, v84, v88
	v_cvt_pk_fp8_f32 v206, v69, v73
	v_cvt_pk_fp8_f32 v207, v85, v89
	v_cvt_pk_fp8_f32 v200, v74, v78 op_sel:[0,0,1]
	v_cvt_pk_fp8_f32 v201, v90, v94 op_sel:[0,0,1]
	v_cvt_pk_fp8_f32 v202, v75, v79 op_sel:[0,0,1]
	v_cvt_pk_fp8_f32 v203, v91, v95 op_sel:[0,0,1]
	v_cvt_pk_fp8_f32 v204, v76, v80 op_sel:[0,0,1]
	v_cvt_pk_fp8_f32 v205, v92, v96 op_sel:[0,0,1]
	v_cvt_pk_fp8_f32 v206, v77, v81 op_sel:[0,0,1]
	v_cvt_pk_fp8_f32 v207, v93, v97 op_sel:[0,0,1]
	s_nop 0
	ds_write2_b64 v140, v[200:201], v[202:203] offset1:16
	ds_write2_b64 v140, v[204:205], v[206:207] offset0:32 offset1:48
	global_load_dwordx4 v[34:37], v130, s[0:1] nt
	global_load_dwordx4 v[38:41], v131, s[0:1] nt
	global_load_dwordx4 v[42:45], v132, s[0:1] nt
	global_load_dwordx4 v[46:49], v133, s[0:1] nt
	global_load_dwordx4 v[50:53], v134, s[0:1] nt
	global_load_dwordx4 v[54:57], v135, s[0:1] nt
	global_load_dwordx4 v[58:61], v136, s[0:1] nt
	global_load_dwordx4 v[62:65], v137, s[0:1] nt
	s_add_u32 s0, s0, 0x10000
	s_addc_u32 s1, s1, 0
	s_branch .Lcvc_s3
	.p2alignl 6, 3212836864

.LBB0_1044:
	s_add_u32 s23, s12, 0x700
	s_addc_u32 s25, s13, 0
	s_and_b64 s[34:35], s[36:37], exec
	s_cselect_b32 s34, s28, s23
	s_cselect_b32 s35, s29, s25
	s_mov_b32 s23, -2
	s_mov_b64 s[40:41], 0x14800000
	ds_write_b128 v252, v[132:135]
	s_branch .LBB0_1046
	.p2alignl 6, 3212836864
